# grid barrier: L1 invalidate issued at arrival (overlaps the wait) instead of after release
# speedup vs baseline: 1.0294x; 1.0294x over previous
.LBB0_69:
	s_lshl_b32 s4, s33, 8
	s_add_u32 s4, s14, s4
	s_addc_u32 s5, s15, 0
	v_mov_b32_e32 v2, 0x1000
	v_mov_b32_e32 v4, 1
	global_atomic_add v4, v2, v4, s[4:5] offset:1024 sc0
	buffer_inv sc1
	v_cvt_f32_u32_e32 v2, v3
	v_sub_u32_e32 v5, 0, v3
	v_rcp_iflag_f32_e32 v2, v2
	s_nop 0
	v_mul_f32_e32 v2, 0x4f7ffffe, v2
	v_cvt_u32_f32_e32 v2, v2
	v_mul_lo_u32 v5, v5, v2
	v_mul_hi_u32 v5, v2, v5
	v_add_u32_e32 v2, v2, v5
	s_waitcnt vmcnt(1)
	v_mul_hi_u32 v2, v4, v2
	v_mul_lo_u32 v5, v2, v3
	v_sub_u32_e32 v5, v4, v5
	v_add_u32_e32 v6, 1, v2
	v_cmp_ge_u32_e32 vcc, v5, v3
	v_add_u32_e32 v4, 1, v4
	s_nop 0
	v_cndmask_b32_e32 v2, v2, v6, vcc
	v_sub_u32_e32 v6, v5, v3
	v_cndmask_b32_e32 v5, v5, v6, vcc
	v_add_u32_e32 v6, 1, v2
	v_cmp_ge_u32_e32 vcc, v5, v3
	s_nop 1
	v_cndmask_b32_e32 v2, v2, v6, vcc
	v_mul_lo_u32 v5, v3, v2
	v_add_u32_e32 v3, v5, v3
	v_cmp_ne_u32_e32 vcc, v4, v3
	s_and_saveexec_b64 s[6:7], vcc
	s_xor_b64 s[6:7], exec, s[6:7]
	s_cbranch_execz .LBB0_83
	s_waitcnt lgkmcnt(0)
	v_mov_b32_e32 v1, 0x2000
	global_load_dword v1, v1, s[4:5] offset:1024 sc1
	s_add_u32 s12, s4, 0x2400
	s_addc_u32 s13, s5, 0
	s_waitcnt vmcnt(0)
	v_cmp_eq_u32_e32 vcc, v1, v2
	s_and_saveexec_b64 s[8:9], vcc
	s_cbranch_execz .LBB0_82
	s_add_u32 s10, s16, 0x4200
	s_addc_u32 s11, s17, 0
	s_mov_b32 s34, 1
	s_mov_b64 s[22:23], 0
	v_mov_b32_e32 v1, 0
	s_branch .LBB0_73

.LBB0_82:
	s_or_b64 exec, exec, s[8:9]
	s_waitcnt vmcnt(0)
	s_nop 0
	s_waitcnt vmcnt(0)

.LBB0_100:
	s_or_b64 exec, exec, s[6:7]
	v_mov_b32_e32 v1, 0x2000
	v_mov_b32_e32 v2, 1
	s_waitcnt vmcnt(0)
	s_nop 0
	global_atomic_add v1, v2, s[4:5] offset:1024
	s_waitcnt vmcnt(0)

.LBB0_103:
	s_or_b64 exec, exec, s[4:5]
	v_readlane_b32 s4, v253, 10
	v_readlane_b32 s5, v253, 11
	s_waitcnt vmcnt(0)
	s_nop 0
	s_nop 2
	global_atomic_add v3, v228, s[4:5]
	s_waitcnt vmcnt(0)

.LBB0_170:
	v_readlane_b32 s4, v253, 8
	v_readlane_b32 s5, v253, 9
	v_cvt_f32_u32_e32 v1, v4
	v_sub_u32_e32 v6, 0, v4
	v_rcp_iflag_f32_e32 v1, v1
	s_nop 1
	global_atomic_add v5, v3, v228, s[4:5] sc0
	buffer_inv sc1
	v_mul_f32_e32 v1, 0x4f7ffffe, v1
	v_cvt_u32_f32_e32 v1, v1
	v_mul_lo_u32 v6, v6, v1
	v_mul_hi_u32 v6, v1, v6
	v_add_u32_e32 v1, v1, v6
	s_waitcnt vmcnt(1)
	v_mul_hi_u32 v1, v5, v1
	v_mul_lo_u32 v6, v1, v4
	v_sub_u32_e32 v6, v5, v6
	v_add_u32_e32 v7, 1, v1
	v_cmp_ge_u32_e32 vcc, v6, v4
	v_add_u32_e32 v5, 1, v5
	s_nop 0
	v_cndmask_b32_e32 v1, v1, v7, vcc
	v_sub_u32_e32 v7, v6, v4
	v_cndmask_b32_e32 v6, v6, v7, vcc
	v_add_u32_e32 v7, 1, v1
	v_cmp_ge_u32_e32 vcc, v6, v4
	s_nop 1
	v_cndmask_b32_e32 v1, v1, v7, vcc
	v_mul_lo_u32 v6, v4, v1
	v_add_u32_e32 v4, v6, v4
	v_cmp_ne_u32_e32 vcc, v5, v4
	s_and_saveexec_b64 s[4:5], vcc
	s_xor_b64 s[4:5], exec, s[4:5]
	s_cbranch_execz .LBB0_184
	v_readlane_b32 s6, v253, 10
	v_readlane_b32 s7, v253, 11
	s_waitcnt lgkmcnt(0)
	s_nop 3
	global_load_dword v2, v3, s[6:7] sc1
	s_waitcnt vmcnt(0)
	v_cmp_eq_u32_e32 vcc, v2, v1
	s_and_saveexec_b64 s[6:7], vcc
	s_cbranch_execz .LBB0_183
	s_mov_b32 s40, 1
	s_mov_b64 s[8:9], 0
	s_branch .LBB0_174

.LBB0_183:
	s_or_b64 exec, exec, s[6:7]
	s_waitcnt vmcnt(0)
	s_nop 0
	s_waitcnt vmcnt(0)

.LBB0_320:
	v_readlane_b32 s4, v253, 8
	v_readlane_b32 s5, v253, 9
	v_cvt_f32_u32_e32 v1, v4
	v_sub_u32_e32 v6, 0, v4
	v_rcp_iflag_f32_e32 v1, v1
	s_nop 1
	global_atomic_add v5, v3, v228, s[4:5] sc0
	buffer_inv sc1
	v_mul_f32_e32 v1, 0x4f7ffffe, v1
	v_cvt_u32_f32_e32 v1, v1
	v_mul_lo_u32 v6, v6, v1
	v_mul_hi_u32 v6, v1, v6
	v_add_u32_e32 v1, v1, v6
	s_waitcnt vmcnt(1)
	v_mul_hi_u32 v1, v5, v1
	v_mul_lo_u32 v6, v1, v4
	v_sub_u32_e32 v6, v5, v6
	v_add_u32_e32 v7, 1, v1
	v_cmp_ge_u32_e32 vcc, v6, v4
	v_add_u32_e32 v5, 1, v5
	s_nop 0
	v_cndmask_b32_e32 v1, v1, v7, vcc
	v_sub_u32_e32 v7, v6, v4
	v_cndmask_b32_e32 v6, v6, v7, vcc
	v_add_u32_e32 v7, 1, v1
	v_cmp_ge_u32_e32 vcc, v6, v4
	s_nop 1
	v_cndmask_b32_e32 v1, v1, v7, vcc
	v_mul_lo_u32 v6, v4, v1
	v_add_u32_e32 v4, v6, v4
	v_cmp_ne_u32_e32 vcc, v5, v4
	s_and_saveexec_b64 s[4:5], vcc
	s_xor_b64 s[4:5], exec, s[4:5]
	s_cbranch_execz .LBB0_334
	v_readlane_b32 s6, v253, 10
	v_readlane_b32 s7, v253, 11
	s_waitcnt lgkmcnt(0)
	s_nop 3
	global_load_dword v2, v3, s[6:7] sc1
	s_waitcnt vmcnt(0)
	v_cmp_eq_u32_e32 vcc, v2, v1
	s_and_saveexec_b64 s[6:7], vcc
	s_cbranch_execz .LBB0_333
	s_mov_b32 s33, 1
	s_mov_b64 s[8:9], 0
	s_branch .LBB0_324

.LBB0_524:
	v_readlane_b32 s4, v253, 8
	v_readlane_b32 s5, v253, 9
	v_cvt_f32_u32_e32 v1, v4
	v_sub_u32_e32 v6, 0, v4
	v_rcp_iflag_f32_e32 v1, v1
	s_nop 1
	global_atomic_add v5, v3, v228, s[4:5] sc0
	buffer_inv sc1
	v_mul_f32_e32 v1, 0x4f7ffffe, v1
	v_cvt_u32_f32_e32 v1, v1
	v_mul_lo_u32 v6, v6, v1
	v_mul_hi_u32 v6, v1, v6
	v_add_u32_e32 v1, v1, v6
	s_waitcnt vmcnt(1)
	v_mul_hi_u32 v1, v5, v1
	v_mul_lo_u32 v6, v1, v4
	v_sub_u32_e32 v6, v5, v6
	v_add_u32_e32 v7, 1, v1
	v_cmp_ge_u32_e32 vcc, v6, v4
	v_add_u32_e32 v5, 1, v5
	s_nop 0
	v_cndmask_b32_e32 v1, v1, v7, vcc
	v_sub_u32_e32 v7, v6, v4
	v_cndmask_b32_e32 v6, v6, v7, vcc
	v_add_u32_e32 v7, 1, v1
	v_cmp_ge_u32_e32 vcc, v6, v4
	s_nop 1
	v_cndmask_b32_e32 v1, v1, v7, vcc
	v_mul_lo_u32 v6, v4, v1
	v_add_u32_e32 v4, v6, v4
	v_cmp_ne_u32_e32 vcc, v5, v4
	s_and_saveexec_b64 s[4:5], vcc
	s_xor_b64 s[4:5], exec, s[4:5]
	s_cbranch_execz .LBB0_538
	v_readlane_b32 s6, v253, 10
	v_readlane_b32 s7, v253, 11
	s_waitcnt lgkmcnt(0)
	s_nop 3
	global_load_dword v2, v3, s[6:7] sc1
	s_waitcnt vmcnt(0)
	v_cmp_eq_u32_e32 vcc, v2, v1
	s_and_saveexec_b64 s[6:7], vcc
	s_cbranch_execz .LBB0_537
	s_mov_b32 s34, 1
	s_mov_b64 s[8:9], 0
	s_branch .LBB0_528
